# prologue rows shared by the 1536 non-pool waves only (pool-item waves take none)
# baseline (speedup 1.0000x reference)
; #define GAS __attribute__((address_space(1)))
; __device__ __forceinline__ void p0_prologue(const Frame& F) {
;     ...
;     const bool is_strip = (role == 1) || (role == 2 && ridx < NSTR - 512);
;     if (!is_strip) {
;         const int NRW = NGW - NSTR;
;         const int rw = role == 0 ? ridx : (role == 3 ? 512 + ridx : 1024 + ridx - (NSTR - 512));
;         for (int m = rw; m < M; m += 2 * NRW) {
;             const int m2 = m + NRW; const bool two = m2 < M;
;             const GAS f32x4* xr = (const GAS f32x4*)(x + (size_t)m * D) + F.lane; const GAS f32x4* xr2 = (const GAS f32x4*)(x + (size_t)(two ? m2 : m) * D) + F.lane; f32x4 v[4], v2[4]; float s = 0.f, s2 = 0.f;
.LBB0_145:
	s_cmpk_lt_i32 s16, 0x180
	s_cselect_b64 s[4:5], -1, 0
	s_load_dwordx2 s[26:27], s[76:77], 0
	s_waitcnt lgkmcnt(0)
	s_and_b32 s3, s100, 3
	s_cmp_eq_u32 s3, 0
	s_cbranch_scc1 .LBB0_161
	s_lshr_b32 s16, s100, 2
	s_mul_i32 s16, s16, 3
	s_add_i32 s16, s16, s3
	s_add_i32 s16, s16, -1
.LBB0_149:
.LBB0_150:
.LBB0_151:
.LBB0_152:
	s_cmpk_gt_i32 s16, 0x3fff
	s_cbranch_scc1 .LBB0_161
	s_waitcnt vmcnt(15)
	v_mbcnt_lo_u32_b32 v2, -1, 0
	v_mbcnt_hi_u32_b32 v2, -1, v2
	v_and_b32_e32 v3, 64, v2
	v_add_u32_e32 v3, 64, v3
	s_waitcnt vmcnt(13)
	v_xor_b32_e32 v4, 1, v2
	v_cmp_lt_i32_e32 vcc, v4, v3
	v_mov_b32_e32 v1, 0
	s_mul_i32 s2, s2, 6
	v_cndmask_b32_e32 v4, v2, v4, vcc
	v_lshlrev_b32_e32 v32, 2, v4
	v_xor_b32_e32 v4, 2, v2
	v_cmp_lt_i32_e32 vcc, v4, v3
	s_mov_b64 s[4:5], 0x5e00000
	v_cndmask_b32_e32 v4, v2, v4, vcc
	v_lshlrev_b32_e32 v33, 2, v4
	v_xor_b32_e32 v4, 4, v2
	v_cmp_lt_i32_e32 vcc, v4, v3
	s_ashr_i32 s17, s16, 31
	s_lshl_b32 s8, s2, 1
	v_cndmask_b32_e32 v4, v2, v4, vcc
	v_lshlrev_b32_e32 v34, 2, v4
	v_xor_b32_e32 v4, 8, v2
	v_cmp_lt_i32_e32 vcc, v4, v3
	s_lshl_b64 s[12:13], s[16:17], 6
	s_mov_b64 s[10:11], 0x7e00000
	v_cndmask_b32_e32 v4, v2, v4, vcc
	v_lshlrev_b32_e32 v35, 2, v4
	v_xor_b32_e32 v4, 16, v2
	v_cmp_lt_i32_e32 vcc, v4, v3
	s_ashr_i32 s9, s8, 31
	s_lshl_b64 s[18:19], s[16:17], 12
	v_cndmask_b32_e32 v4, v2, v4, vcc
	v_lshlrev_b32_e32 v36, 2, v4
	v_xor_b32_e32 v4, 32, v2
	v_cmp_lt_i32_e32 vcc, v4, v3
	v_mov_b32_e32 v3, v1
	v_lshlrev_b32_e32 v0, 4, v68
	v_cndmask_b32_e32 v2, v2, v4, vcc
	v_lshlrev_b32_e32 v37, 2, v2
	v_lshlrev_b32_e32 v2, 3, v68
	v_lshl_add_u64 v[4:5], s[14:15], 0, v[2:3]
	s_waitcnt vmcnt(9)
	v_lshl_add_u64 v[22:23], v[4:5], 0, s[4:5]
	v_lshlrev_b32_e32 v4, 2, v68
	v_mov_b32_e32 v5, v1
	v_lshl_add_u64 v[6:7], s[14:15], 0, v[4:5]
	v_lshl_add_u64 v[4:5], s[12:13], 0, v[4:5]
	s_lshl_b64 s[12:13], s[16:17], 11
	v_lshl_add_u64 v[24:25], v[6:7], 0, s[10:11]
	v_lshl_add_u64 v[26:27], v[4:5], 0, s[10:11]
	s_lshl_b64 s[10:11], s[8:9], 6
	s_waitcnt vmcnt(8)
	v_or_b32_e32 v28, s12, v2
	v_mov_b32_e32 v29, s13
	s_lshl_b64 s[12:13], s[8:9], 11
	s_add_u32 s18, s26, s18
	s_addc_u32 s19, s27, s19
	v_lshl_add_u64 v[20:21], s[26:27], 0, v[0:1]
	v_lshl_add_u64 v[0:1], s[18:19], 0, v[0:1]
	s_mov_b64 s[18:19], 0x800
	v_cmp_gt_u32_e64 s[4:5], 16, v68
	v_cmp_eq_u32_e64 s[6:7], 0, v68
	v_lshl_add_u64 v[30:31], v[0:1], 0, s[18:19]
	s_lshl_b64 s[18:19], s[8:9], 12
	s_movk_i32 s3, 0x7fff
	s_mov_b32 s9, 0xffff0000
	s_mov_b32 s17, 0x5e00000
	s_branch .LBB0_156
